# P23: epilogue of the acc[0] rows issued inside the last K-iteration (segment 4 load part + between its MFMAs)
# speedup vs baseline: 1.0219x; 1.0047x over previous
.Ltx23_skip:
	ds_read_b128 v[2:5], v184
	ds_read_b128 v[6:9], v185
	ds_read_b128 v[10:13], v192
	ds_read_b128 v[14:17], v193
	ds_read_b128 v[18:21], v186
	ds_read_b128 v[22:25], v187
	ds_read_b128 v[26:29], v194
	ds_read_b128 v[30:33], v195
	v_mov_b32_e32 v172, v176
	ds_read_b128 v[164:167], v196 offset:32768
	ds_read_b128 v[168:171], v196 offset:33792
	ds_read_b128 v[198:201], v196 offset:34816
	ds_read_b128 v[202:205], v196 offset:35840
	ds_read_b128 v[214:217], v196 offset:36864
	ds_read_b128 v[218:221], v196 offset:37888
	ds_read_b128 v[222:225], v196 offset:38912
	ds_read_b128 v[226:229], v196 offset:39936
	s_add_i32 s86, s86, s47
	s_mov_b32 m0, s55
	v_add_u32_e32 v172, s86, v172
	global_load_lds_dwordx4 v172, s[4:5]
	v_mov_b32_e32 v172, v176
	s_add_i32 s86, s86, s47
	v_add_u32_e32 v172, s86, v172
	s_mov_b32 m0, s56
	s_nop 0
	global_load_lds_dwordx4 v172, s[4:5]
	s_waitcnt vmcnt(8)
	s_waitcnt lgkmcnt(0)
	s_barrier
	s_setprio 1
	s_waitcnt lgkmcnt(0)
	v_mfma_f32_16x16x128_f8f6f4 v[158:161], v[2:9], v[164:171], v[158:161]
	v_mfma_f32_16x16x128_f8f6f4 v[154:157], v[10:17], v[164:171], v[154:157]
	v_mfma_f32_16x16x128_f8f6f4 v[150:153], v[2:9], v[198:205], v[150:153]
	v_mfma_f32_16x16x128_f8f6f4 v[146:149], v[10:17], v[198:205], v[146:149]
	v_mfma_f32_16x16x128_f8f6f4 v[138:141], v[2:9], v[214:221], v[138:141]
	v_mfma_f32_16x16x128_f8f6f4 v[130:133], v[10:17], v[214:221], v[130:133]
	v_mfma_f32_16x16x128_f8f6f4 v[122:125], v[2:9], v[222:229], v[122:125]
	v_mfma_f32_16x16x128_f8f6f4 v[114:117], v[10:17], v[222:229], v[114:117]
	s_setprio 0
	s_setprio 1
	v_mfma_f32_16x16x128_f8f6f4 v[142:145], v[18:25], v[164:171], v[142:145]
	v_mfma_f32_16x16x128_f8f6f4 v[134:137], v[26:33], v[164:171], v[134:137]
	v_mfma_f32_16x16x128_f8f6f4 v[126:129], v[18:25], v[198:205], v[126:129]
	v_mfma_f32_16x16x128_f8f6f4 v[118:121], v[26:33], v[198:205], v[118:121]
	v_mfma_f32_16x16x128_f8f6f4 v[110:113], v[18:25], v[214:221], v[110:113]
	v_mfma_f32_16x16x128_f8f6f4 v[106:109], v[26:33], v[214:221], v[106:109]
	v_mfma_f32_16x16x128_f8f6f4 v[102:105], v[18:25], v[222:229], v[102:105]
	v_mfma_f32_16x16x128_f8f6f4 v[98:101], v[26:33], v[222:229], v[98:101]
	s_setprio 0
	s_barrier
	s_cmp_eq_u32 s67, s83
	s_cbranch_scc1 .Lh23_last
	v_mov_b32_e32 v172, v177
	ds_read_b128 v[164:167], v196 offset:49152
	ds_read_b128 v[168:171], v196 offset:50176
	ds_read_b128 v[198:201], v196 offset:51200
	ds_read_b128 v[202:205], v196 offset:52224
	ds_read_b128 v[214:217], v196 offset:53248
	ds_read_b128 v[218:221], v196 offset:54272
	ds_read_b128 v[222:225], v196 offset:55296
	ds_read_b128 v[226:229], v196 offset:56320
	s_mov_b32 m0, s58
	v_add_u32_e32 v172, s85, v172
	global_load_lds_dwordx4 v172, s[6:7]
	v_mov_b32_e32 v172, v177
	s_add_i32 s85, s85, s48
	v_add_u32_e32 v172, s85, v172
	s_mov_b32 m0, s59
	s_add_i32 s85, s85, s48
	global_load_lds_dwordx4 v172, s[6:7]
	v_mov_b32_e32 v172, v177
	s_mov_b32 m0, s62
	v_add_u32_e32 v172, s85, v172
	global_load_lds_dwordx4 v172, s[6:7]
	v_mov_b32_e32 v172, v177
	s_add_i32 s85, s85, s48
	v_add_u32_e32 v172, s85, v172
	s_mov_b32 m0, s63
	s_nop 0
	global_load_lds_dwordx4 v172, s[6:7]
	v_mov_b32_e32 v172, v176
	s_mov_b32 m0, s60
	v_add_u32_e32 v172, s84, v172
	global_load_lds_dwordx4 v172, s[4:5]
	v_mov_b32_e32 v172, v176
	s_add_i32 s84, s84, s47
	v_add_u32_e32 v172, s84, v172
	s_mov_b32 m0, s61
	s_nop 0
	global_load_lds_dwordx4 v172, s[4:5]
	s_waitcnt vmcnt(8)
	s_waitcnt lgkmcnt(0)
	s_barrier
	s_setprio 1
	s_waitcnt lgkmcnt(0)
	v_mfma_f32_16x16x128_f8f6f4 v[94:97], v[2:9], v[164:171], v[94:97]
	v_mfma_f32_16x16x128_f8f6f4 v[90:93], v[10:17], v[164:171], v[90:93]
	v_mfma_f32_16x16x128_f8f6f4 v[86:89], v[2:9], v[198:205], v[86:89]
	v_mfma_f32_16x16x128_f8f6f4 v[82:85], v[10:17], v[198:205], v[82:85]
	v_mfma_f32_16x16x128_f8f6f4 v[74:77], v[2:9], v[214:221], v[74:77]
	v_mfma_f32_16x16x128_f8f6f4 v[66:69], v[10:17], v[214:221], v[66:69]
	v_mfma_f32_16x16x128_f8f6f4 v[58:61], v[2:9], v[222:229], v[58:61]
	v_mfma_f32_16x16x128_f8f6f4 v[50:53], v[10:17], v[222:229], v[50:53]
	s_setprio 0
	s_setprio 1
	v_mfma_f32_16x16x128_f8f6f4 v[78:81], v[18:25], v[164:171], v[78:81]
	v_mfma_f32_16x16x128_f8f6f4 v[70:73], v[26:33], v[164:171], v[70:73]
	v_mfma_f32_16x16x128_f8f6f4 v[62:65], v[18:25], v[198:205], v[62:65]
	v_mfma_f32_16x16x128_f8f6f4 v[54:57], v[26:33], v[198:205], v[54:57]
	v_mfma_f32_16x16x128_f8f6f4 v[46:49], v[18:25], v[214:221], v[46:49]
	v_mfma_f32_16x16x128_f8f6f4 v[42:45], v[26:33], v[214:221], v[42:45]
	v_mfma_f32_16x16x128_f8f6f4 v[38:41], v[18:25], v[222:229], v[38:41]
	v_mfma_f32_16x16x128_f8f6f4 v[34:37], v[26:33], v[222:229], v[34:37]
	s_setprio 0
	s_barrier
	s_add_i32 s83, s83, 2
	s_addk_i32 s28, 0x100
	s_addk_i32 s82, 0x100
	s_cmp_ge_i32 s83, s64
	s_cbranch_scc0 .LBB0_2937
	s_branch .LBB0_2939
.Lh23_last:
	v_mov_b32_e32 v172, v177
	ds_read_b128 v[164:167], v196 offset:49152
	ds_read_b128 v[168:171], v196 offset:50176
	ds_read_b128 v[198:201], v196 offset:51200
	ds_read_b128 v[202:205], v196 offset:52224
	ds_read_b128 v[214:217], v196 offset:53248
	ds_read_b128 v[218:221], v196 offset:54272
	ds_read_b128 v[222:225], v196 offset:55296
	ds_read_b128 v[226:229], v196 offset:56320
	s_mov_b32 m0, s58
	v_add_u32_e32 v172, s85, v172
	global_load_lds_dwordx4 v172, s[6:7]
	v_mov_b32_e32 v172, v177
	s_add_i32 s85, s85, s48
	v_add_u32_e32 v172, s85, v172
	s_mov_b32 m0, s59
	s_add_i32 s85, s85, s48
	global_load_lds_dwordx4 v172, s[6:7]
	v_mov_b32_e32 v172, v177
	s_mov_b32 m0, s62
	v_add_u32_e32 v172, s85, v172
	global_load_lds_dwordx4 v172, s[6:7]
	v_mov_b32_e32 v172, v177
	s_add_i32 s85, s85, s48
	v_add_u32_e32 v172, s85, v172
	s_mov_b32 m0, s63
	s_nop 0
	global_load_lds_dwordx4 v172, s[6:7]
	v_mov_b32_e32 v172, v176
	s_mov_b32 m0, s60
	v_add_u32_e32 v172, s84, v172
	global_load_lds_dwordx4 v172, s[4:5]
	v_mov_b32_e32 v172, v176
	s_add_i32 s84, s84, s47
	v_add_u32_e32 v172, s84, v172
	s_mov_b32 m0, s61
	s_nop 0
	global_load_lds_dwordx4 v172, s[4:5]
	s_mul_hi_i32 s25, s81, 0x2e8ba2e9
	s_lshr_b32 s28, s25, 31
	s_lshr_b32 s25, s25, 3
	s_add_i32 s25, s25, s28
	s_mul_i32 s25, s25, 44
	s_sub_i32 s25, s81, s25
	s_lshl_b32 s28, s25, 7
	s_lshl_b32 s24, s24, 8
	s_add_i32 s24, s24, s66
	s_mul_i32 s24, s24, s71
	s_add_i32 s24, s24, s28
	s_add_i32 s24, s24, s8
	s_add_u32 s100, s12, s24
	s_addc_u32 s101, s13, 0
	s_mov_b32 s98, 0xbfb8aa3b
	v_mul_u32_u24_e32 v206, s71, v178
	v_lshl_add_u32 v206, v179, 3, v206
	v_pk_fma_f32 v[158:159], v[158:159], s[18:19], 0 op_sel_hi:[1,0,0]
	v_pk_fma_f32 v[160:161], v[160:161], s[18:19], 0 op_sel_hi:[1,0,0]
	v_pk_fma_f32 v[154:155], v[154:155], s[18:19], 0 op_sel_hi:[1,0,0]
	v_pk_fma_f32 v[156:157], v[156:157], s[18:19], 0 op_sel_hi:[1,0,0]
	v_pk_fma_f32 v[142:143], v[142:143], s[20:21], 0 op_sel_hi:[1,0,0]
	v_pk_fma_f32 v[144:145], v[144:145], s[20:21], 0 op_sel_hi:[1,0,0]
	v_pk_fma_f32 v[134:135], v[134:135], s[20:21], 0 op_sel_hi:[1,0,0]
	v_pk_fma_f32 v[136:137], v[136:137], s[20:21], 0 op_sel_hi:[1,0,0]
	v_pk_fma_f32 v[150:151], v[150:151], s[18:19], 0 op_sel_hi:[1,0,0]
	v_pk_fma_f32 v[152:153], v[152:153], s[18:19], 0 op_sel_hi:[1,0,0]
	v_pk_fma_f32 v[146:147], v[146:147], s[18:19], 0 op_sel_hi:[1,0,0]
	v_pk_fma_f32 v[148:149], v[148:149], s[18:19], 0 op_sel_hi:[1,0,0]
	v_pk_fma_f32 v[126:127], v[126:127], s[20:21], 0 op_sel_hi:[1,0,0]
	v_pk_fma_f32 v[128:129], v[128:129], s[20:21], 0 op_sel_hi:[1,0,0]
	v_pk_fma_f32 v[118:119], v[118:119], s[20:21], 0 op_sel_hi:[1,0,0]
	v_pk_fma_f32 v[120:121], v[120:121], s[20:21], 0 op_sel_hi:[1,0,0]
	v_pk_mul_f32 v[230:231], v[158:159], s[98:99] op_sel_hi:[1,0]
	v_pk_mul_f32 v[232:233], v[160:161], s[98:99] op_sel_hi:[1,0]
	v_pk_mul_f32 v[234:235], v[154:155], s[98:99] op_sel_hi:[1,0]
	v_pk_mul_f32 v[236:237], v[156:157], s[98:99] op_sel_hi:[1,0]
	v_pk_mul_f32 v[238:239], v[150:151], s[98:99] op_sel_hi:[1,0]
	v_pk_mul_f32 v[240:241], v[152:153], s[98:99] op_sel_hi:[1,0]
	v_pk_mul_f32 v[242:243], v[146:147], s[98:99] op_sel_hi:[1,0]
	v_pk_mul_f32 v[244:245], v[148:149], s[98:99] op_sel_hi:[1,0]
	v_exp_f32_e32 v230, v230
	v_exp_f32_e32 v231, v231
	v_exp_f32_e32 v232, v232
	v_exp_f32_e32 v233, v233
	v_exp_f32_e32 v234, v234
	v_exp_f32_e32 v235, v235
	v_exp_f32_e32 v236, v236
	v_exp_f32_e32 v237, v237
	v_exp_f32_e32 v238, v238
	v_exp_f32_e32 v239, v239
	v_exp_f32_e32 v240, v240
	v_exp_f32_e32 v241, v241
	v_exp_f32_e32 v242, v242
	v_exp_f32_e32 v243, v243
	v_exp_f32_e32 v244, v244
	v_exp_f32_e32 v245, v245
	v_pk_add_f32 v[230:231], v[230:231], 1.0 op_sel_hi:[1,0]
	v_pk_add_f32 v[232:233], v[232:233], 1.0 op_sel_hi:[1,0]
	v_pk_add_f32 v[234:235], v[234:235], 1.0 op_sel_hi:[1,0]
	v_pk_add_f32 v[236:237], v[236:237], 1.0 op_sel_hi:[1,0]
	v_pk_add_f32 v[238:239], v[238:239], 1.0 op_sel_hi:[1,0]
	v_pk_add_f32 v[240:241], v[240:241], 1.0 op_sel_hi:[1,0]
	v_pk_add_f32 v[242:243], v[242:243], 1.0 op_sel_hi:[1,0]
	v_pk_add_f32 v[244:245], v[244:245], 1.0 op_sel_hi:[1,0]
	v_rcp_f32_e32 v230, v230
	v_rcp_f32_e32 v231, v231
	v_rcp_f32_e32 v232, v232
	v_rcp_f32_e32 v233, v233
	v_rcp_f32_e32 v234, v234
	v_rcp_f32_e32 v235, v235
	v_rcp_f32_e32 v236, v236
	v_rcp_f32_e32 v237, v237
	v_rcp_f32_e32 v238, v238
	v_rcp_f32_e32 v239, v239
	v_rcp_f32_e32 v240, v240
	v_rcp_f32_e32 v241, v241
	v_rcp_f32_e32 v242, v242
	v_rcp_f32_e32 v243, v243
	v_rcp_f32_e32 v244, v244
	v_rcp_f32_e32 v245, v245
	v_pk_mul_f32 v[230:231], v[158:159], v[230:231]
	v_pk_mul_f32 v[232:233], v[160:161], v[232:233]
	v_pk_mul_f32 v[234:235], v[154:155], v[234:235]
	v_pk_mul_f32 v[236:237], v[156:157], v[236:237]
	v_pk_mul_f32 v[238:239], v[150:151], v[238:239]
	v_pk_mul_f32 v[240:241], v[152:153], v[240:241]
	v_pk_mul_f32 v[242:243], v[146:147], v[242:243]
	v_pk_mul_f32 v[244:245], v[148:149], v[244:245]
	v_pk_mul_f32 v[142:143], v[142:143], v[230:231]
	v_pk_mul_f32 v[144:145], v[144:145], v[232:233]
	v_pk_mul_f32 v[134:135], v[134:135], v[234:235]
	v_pk_mul_f32 v[136:137], v[136:137], v[236:237]
	v_pk_mul_f32 v[126:127], v[126:127], v[238:239]
	v_pk_mul_f32 v[128:129], v[128:129], v[240:241]
	v_pk_mul_f32 v[118:119], v[118:119], v[242:243]
	v_pk_mul_f32 v[120:121], v[120:121], v[244:245]
	v_med3_f32 v142, v142, s72, v197
	v_med3_f32 v143, v143, s72, v197
	v_med3_f32 v144, v144, s72, v197
	v_med3_f32 v145, v145, s72, v197
	v_med3_f32 v134, v134, s72, v197
	v_med3_f32 v135, v135, s72, v197
	v_med3_f32 v136, v136, s72, v197
	v_med3_f32 v137, v137, s72, v197
	v_med3_f32 v126, v126, s72, v197
	v_med3_f32 v127, v127, s72, v197
	v_med3_f32 v128, v128, s72, v197
	v_med3_f32 v129, v129, s72, v197
	v_med3_f32 v118, v118, s72, v197
	v_med3_f32 v119, v119, s72, v197
	v_med3_f32 v120, v120, s72, v197
	v_med3_f32 v121, v121, s72, v197
	v_cvt_pk_fp8_f32 v246, v142, v143
	v_cvt_pk_fp8_f32 v247, v134, v135
	v_cvt_pk_fp8_f32 v248, v126, v127
	v_cvt_pk_fp8_f32 v249, v118, v119
	v_add_u32_e32 v208, s57, v206
	v_cvt_pk_fp8_f32 v246, v144, v145 op_sel:[0,0,1]
	v_cvt_pk_fp8_f32 v247, v136, v137 op_sel:[0,0,1]
	v_cvt_pk_fp8_f32 v248, v128, v129 op_sel:[0,0,1]
	v_cvt_pk_fp8_f32 v249, v120, v121 op_sel:[0,0,1]
	s_nop 1
	global_store_dwordx2 v206, v[246:247], s[100:101]
	global_store_dwordx2 v208, v[248:249], s[100:101]
	s_waitcnt vmcnt(10)
	s_waitcnt lgkmcnt(0)
	s_barrier
	s_setprio 1
	s_waitcnt lgkmcnt(0)
	v_mfma_f32_16x16x128_f8f6f4 v[94:97], v[2:9], v[164:171], v[94:97]
	v_pk_fma_f32 v[138:139], v[138:139], s[18:19], 0 op_sel_hi:[1,0,0]
	v_pk_fma_f32 v[140:141], v[140:141], s[18:19], 0 op_sel_hi:[1,0,0]
	v_pk_fma_f32 v[130:131], v[130:131], s[18:19], 0 op_sel_hi:[1,0,0]
	v_pk_fma_f32 v[132:133], v[132:133], s[18:19], 0 op_sel_hi:[1,0,0]
	v_pk_fma_f32 v[110:111], v[110:111], s[20:21], 0 op_sel_hi:[1,0,0]
	v_pk_fma_f32 v[112:113], v[112:113], s[20:21], 0 op_sel_hi:[1,0,0]
	v_pk_fma_f32 v[106:107], v[106:107], s[20:21], 0 op_sel_hi:[1,0,0]
	v_mfma_f32_16x16x128_f8f6f4 v[90:93], v[10:17], v[164:171], v[90:93]
	v_pk_fma_f32 v[108:109], v[108:109], s[20:21], 0 op_sel_hi:[1,0,0]
	v_pk_fma_f32 v[122:123], v[122:123], s[18:19], 0 op_sel_hi:[1,0,0]
	v_pk_fma_f32 v[124:125], v[124:125], s[18:19], 0 op_sel_hi:[1,0,0]
	v_pk_fma_f32 v[114:115], v[114:115], s[18:19], 0 op_sel_hi:[1,0,0]
	v_pk_fma_f32 v[116:117], v[116:117], s[18:19], 0 op_sel_hi:[1,0,0]
	v_pk_fma_f32 v[102:103], v[102:103], s[20:21], 0 op_sel_hi:[1,0,0]
	v_pk_fma_f32 v[104:105], v[104:105], s[20:21], 0 op_sel_hi:[1,0,0]
	v_mfma_f32_16x16x128_f8f6f4 v[86:89], v[2:9], v[198:205], v[86:89]
	v_pk_fma_f32 v[98:99], v[98:99], s[20:21], 0 op_sel_hi:[1,0,0]
	v_pk_fma_f32 v[100:101], v[100:101], s[20:21], 0 op_sel_hi:[1,0,0]
	v_pk_mul_f32 v[230:231], v[138:139], s[98:99] op_sel_hi:[1,0]
	v_pk_mul_f32 v[232:233], v[140:141], s[98:99] op_sel_hi:[1,0]
	v_pk_mul_f32 v[234:235], v[130:131], s[98:99] op_sel_hi:[1,0]
	v_pk_mul_f32 v[236:237], v[132:133], s[98:99] op_sel_hi:[1,0]
	v_pk_mul_f32 v[238:239], v[122:123], s[98:99] op_sel_hi:[1,0]
	v_mfma_f32_16x16x128_f8f6f4 v[82:85], v[10:17], v[198:205], v[82:85]
	v_pk_mul_f32 v[240:241], v[124:125], s[98:99] op_sel_hi:[1,0]
	v_pk_mul_f32 v[242:243], v[114:115], s[98:99] op_sel_hi:[1,0]
	v_pk_mul_f32 v[244:245], v[116:117], s[98:99] op_sel_hi:[1,0]
	v_exp_f32_e32 v230, v230
	v_exp_f32_e32 v231, v231
	v_exp_f32_e32 v232, v232
	v_exp_f32_e32 v233, v233
	v_mfma_f32_16x16x128_f8f6f4 v[74:77], v[2:9], v[214:221], v[74:77]
	v_exp_f32_e32 v234, v234
	v_exp_f32_e32 v235, v235
	v_exp_f32_e32 v236, v236
	v_exp_f32_e32 v237, v237
	v_exp_f32_e32 v238, v238
	v_exp_f32_e32 v239, v239
	v_exp_f32_e32 v240, v240
	v_mfma_f32_16x16x128_f8f6f4 v[66:69], v[10:17], v[214:221], v[66:69]
	v_exp_f32_e32 v241, v241
	v_exp_f32_e32 v242, v242
	v_exp_f32_e32 v243, v243
	v_exp_f32_e32 v244, v244
	v_exp_f32_e32 v245, v245
	v_pk_add_f32 v[230:231], v[230:231], 1.0 op_sel_hi:[1,0]
	v_pk_add_f32 v[232:233], v[232:233], 1.0 op_sel_hi:[1,0]
	v_mfma_f32_16x16x128_f8f6f4 v[58:61], v[2:9], v[222:229], v[58:61]
	v_pk_add_f32 v[234:235], v[234:235], 1.0 op_sel_hi:[1,0]
	v_pk_add_f32 v[236:237], v[236:237], 1.0 op_sel_hi:[1,0]
	v_pk_add_f32 v[238:239], v[238:239], 1.0 op_sel_hi:[1,0]
	v_pk_add_f32 v[240:241], v[240:241], 1.0 op_sel_hi:[1,0]
	v_pk_add_f32 v[242:243], v[242:243], 1.0 op_sel_hi:[1,0]
	v_pk_add_f32 v[244:245], v[244:245], 1.0 op_sel_hi:[1,0]
	v_rcp_f32_e32 v230, v230
	v_mfma_f32_16x16x128_f8f6f4 v[50:53], v[10:17], v[222:229], v[50:53]
	v_rcp_f32_e32 v231, v231
	v_rcp_f32_e32 v232, v232
	v_rcp_f32_e32 v233, v233
	v_rcp_f32_e32 v234, v234
	v_rcp_f32_e32 v235, v235
	v_rcp_f32_e32 v236, v236
	v_rcp_f32_e32 v237, v237
	s_setprio 0
	s_setprio 1
	v_mfma_f32_16x16x128_f8f6f4 v[78:81], v[18:25], v[164:171], v[78:81]
	v_rcp_f32_e32 v238, v238
	v_rcp_f32_e32 v239, v239
	v_rcp_f32_e32 v240, v240
	v_rcp_f32_e32 v241, v241
	v_rcp_f32_e32 v242, v242
	v_rcp_f32_e32 v243, v243
	v_rcp_f32_e32 v244, v244
	v_mfma_f32_16x16x128_f8f6f4 v[70:73], v[26:33], v[164:171], v[70:73]
	v_rcp_f32_e32 v245, v245
	v_pk_mul_f32 v[230:231], v[138:139], v[230:231]
	v_pk_mul_f32 v[232:233], v[140:141], v[232:233]
	v_pk_mul_f32 v[234:235], v[130:131], v[234:235]
	v_pk_mul_f32 v[236:237], v[132:133], v[236:237]
	v_pk_mul_f32 v[238:239], v[122:123], v[238:239]
	v_pk_mul_f32 v[240:241], v[124:125], v[240:241]
	v_mfma_f32_16x16x128_f8f6f4 v[62:65], v[18:25], v[198:205], v[62:65]
	v_pk_mul_f32 v[242:243], v[114:115], v[242:243]
	v_pk_mul_f32 v[244:245], v[116:117], v[244:245]
	v_pk_mul_f32 v[110:111], v[110:111], v[230:231]
	v_pk_mul_f32 v[112:113], v[112:113], v[232:233]
	v_pk_mul_f32 v[106:107], v[106:107], v[234:235]
	v_pk_mul_f32 v[108:109], v[108:109], v[236:237]
	v_pk_mul_f32 v[102:103], v[102:103], v[238:239]
	v_mfma_f32_16x16x128_f8f6f4 v[54:57], v[26:33], v[198:205], v[54:57]
	v_pk_mul_f32 v[104:105], v[104:105], v[240:241]
	v_pk_mul_f32 v[98:99], v[98:99], v[242:243]
	v_pk_mul_f32 v[100:101], v[100:101], v[244:245]
	v_med3_f32 v110, v110, s72, v197
	v_med3_f32 v111, v111, s72, v197
	v_med3_f32 v112, v112, s72, v197
	v_med3_f32 v113, v113, s72, v197
	v_mfma_f32_16x16x128_f8f6f4 v[46:49], v[18:25], v[214:221], v[46:49]
	v_med3_f32 v106, v106, s72, v197
	v_med3_f32 v107, v107, s72, v197
	v_med3_f32 v108, v108, s72, v197
	v_med3_f32 v109, v109, s72, v197
	v_med3_f32 v102, v102, s72, v197
	v_med3_f32 v103, v103, s72, v197
	v_med3_f32 v104, v104, s72, v197
	v_mfma_f32_16x16x128_f8f6f4 v[42:45], v[26:33], v[214:221], v[42:45]
	v_med3_f32 v105, v105, s72, v197
	v_med3_f32 v98, v98, s72, v197
	v_med3_f32 v99, v99, s72, v197
	v_med3_f32 v100, v100, s72, v197
	v_med3_f32 v101, v101, s72, v197
	v_cvt_pk_fp8_f32 v246, v110, v111
	v_cvt_pk_fp8_f32 v247, v106, v107
	v_mfma_f32_16x16x128_f8f6f4 v[38:41], v[18:25], v[222:229], v[38:41]
	v_cvt_pk_fp8_f32 v248, v102, v103
	v_cvt_pk_fp8_f32 v249, v98, v99
	v_add_u32_e32 v207, s73, v206
	v_add_u32_e32 v208, s74, v206
	v_cvt_pk_fp8_f32 v246, v112, v113 op_sel:[0,0,1]
	v_cvt_pk_fp8_f32 v247, v108, v109 op_sel:[0,0,1]
	v_cvt_pk_fp8_f32 v248, v104, v105 op_sel:[0,0,1]
	v_mfma_f32_16x16x128_f8f6f4 v[34:37], v[26:33], v[222:229], v[34:37]
	v_cvt_pk_fp8_f32 v249, v100, v101 op_sel:[0,0,1]
	s_nop 1
	global_store_dwordx2 v207, v[246:247], s[100:101]
	global_store_dwordx2 v208, v[248:249], s[100:101]
	s_setprio 0
	s_barrier
	s_and_b64 vcc, exec, s[16:17]
	s_cbranch_vccz .Lh23_nb
	s_barrier
.Lh23_nb:
	s_nop 15
	s_nop 15
	s_branch .Lh23_epi1

.Lh23_epi1:
	v_pk_fma_f32 v[94:95], v[94:95], s[18:19], 0 op_sel_hi:[1,0,0]
	v_pk_fma_f32 v[96:97], v[96:97], s[18:19], 0 op_sel_hi:[1,0,0]
	v_pk_fma_f32 v[90:91], v[90:91], s[18:19], 0 op_sel_hi:[1,0,0]
	v_pk_fma_f32 v[92:93], v[92:93], s[18:19], 0 op_sel_hi:[1,0,0]
	v_pk_fma_f32 v[78:79], v[78:79], s[20:21], 0 op_sel_hi:[1,0,0]
	v_pk_fma_f32 v[80:81], v[80:81], s[20:21], 0 op_sel_hi:[1,0,0]
	v_pk_fma_f32 v[70:71], v[70:71], s[20:21], 0 op_sel_hi:[1,0,0]
	v_pk_fma_f32 v[72:73], v[72:73], s[20:21], 0 op_sel_hi:[1,0,0]
	v_pk_fma_f32 v[86:87], v[86:87], s[18:19], 0 op_sel_hi:[1,0,0]
	v_pk_fma_f32 v[88:89], v[88:89], s[18:19], 0 op_sel_hi:[1,0,0]
	v_pk_fma_f32 v[82:83], v[82:83], s[18:19], 0 op_sel_hi:[1,0,0]
	v_pk_fma_f32 v[84:85], v[84:85], s[18:19], 0 op_sel_hi:[1,0,0]
	v_pk_fma_f32 v[62:63], v[62:63], s[20:21], 0 op_sel_hi:[1,0,0]
	v_pk_fma_f32 v[64:65], v[64:65], s[20:21], 0 op_sel_hi:[1,0,0]
	v_pk_fma_f32 v[54:55], v[54:55], s[20:21], 0 op_sel_hi:[1,0,0]
	v_pk_fma_f32 v[56:57], v[56:57], s[20:21], 0 op_sel_hi:[1,0,0]
	v_pk_mul_f32 v[230:231], v[94:95], s[98:99] op_sel_hi:[1,0]
	v_pk_mul_f32 v[232:233], v[96:97], s[98:99] op_sel_hi:[1,0]
	v_pk_mul_f32 v[234:235], v[90:91], s[98:99] op_sel_hi:[1,0]
	v_pk_mul_f32 v[236:237], v[92:93], s[98:99] op_sel_hi:[1,0]
	v_pk_mul_f32 v[238:239], v[86:87], s[98:99] op_sel_hi:[1,0]
	v_pk_mul_f32 v[240:241], v[88:89], s[98:99] op_sel_hi:[1,0]
	v_pk_mul_f32 v[242:243], v[82:83], s[98:99] op_sel_hi:[1,0]
	v_pk_mul_f32 v[244:245], v[84:85], s[98:99] op_sel_hi:[1,0]
	v_exp_f32_e32 v230, v230
	v_exp_f32_e32 v231, v231
	v_exp_f32_e32 v232, v232
	v_exp_f32_e32 v233, v233
	v_exp_f32_e32 v234, v234
	v_exp_f32_e32 v235, v235
	v_exp_f32_e32 v236, v236
	v_exp_f32_e32 v237, v237
	v_exp_f32_e32 v238, v238
	v_exp_f32_e32 v239, v239
	v_exp_f32_e32 v240, v240
	v_exp_f32_e32 v241, v241
	v_exp_f32_e32 v242, v242
	v_exp_f32_e32 v243, v243
	v_exp_f32_e32 v244, v244
	v_exp_f32_e32 v245, v245
	v_pk_add_f32 v[230:231], v[230:231], 1.0 op_sel_hi:[1,0]
	v_pk_add_f32 v[232:233], v[232:233], 1.0 op_sel_hi:[1,0]
	v_pk_add_f32 v[234:235], v[234:235], 1.0 op_sel_hi:[1,0]
	v_pk_add_f32 v[236:237], v[236:237], 1.0 op_sel_hi:[1,0]
	v_pk_add_f32 v[238:239], v[238:239], 1.0 op_sel_hi:[1,0]
	v_pk_add_f32 v[240:241], v[240:241], 1.0 op_sel_hi:[1,0]
	v_pk_add_f32 v[242:243], v[242:243], 1.0 op_sel_hi:[1,0]
	v_pk_add_f32 v[244:245], v[244:245], 1.0 op_sel_hi:[1,0]
	v_rcp_f32_e32 v230, v230
	v_rcp_f32_e32 v231, v231
	v_rcp_f32_e32 v232, v232
	v_rcp_f32_e32 v233, v233
	v_rcp_f32_e32 v234, v234
	v_rcp_f32_e32 v235, v235
	v_rcp_f32_e32 v236, v236
	v_rcp_f32_e32 v237, v237
	v_rcp_f32_e32 v238, v238
	v_rcp_f32_e32 v239, v239
	v_rcp_f32_e32 v240, v240
	v_rcp_f32_e32 v241, v241
	v_rcp_f32_e32 v242, v242
	v_rcp_f32_e32 v243, v243
	v_rcp_f32_e32 v244, v244
	v_rcp_f32_e32 v245, v245
	v_pk_mul_f32 v[230:231], v[94:95], v[230:231]
	v_pk_mul_f32 v[232:233], v[96:97], v[232:233]
	v_pk_mul_f32 v[234:235], v[90:91], v[234:235]
	v_pk_mul_f32 v[236:237], v[92:93], v[236:237]
	v_pk_mul_f32 v[238:239], v[86:87], v[238:239]
	v_pk_mul_f32 v[240:241], v[88:89], v[240:241]
	v_pk_mul_f32 v[242:243], v[82:83], v[242:243]
	v_pk_mul_f32 v[244:245], v[84:85], v[244:245]
	v_pk_mul_f32 v[78:79], v[78:79], v[230:231]
	v_pk_mul_f32 v[80:81], v[80:81], v[232:233]
	v_pk_mul_f32 v[70:71], v[70:71], v[234:235]
	v_pk_mul_f32 v[72:73], v[72:73], v[236:237]
	v_pk_mul_f32 v[62:63], v[62:63], v[238:239]
	v_pk_mul_f32 v[64:65], v[64:65], v[240:241]
	v_pk_mul_f32 v[54:55], v[54:55], v[242:243]
	v_pk_mul_f32 v[56:57], v[56:57], v[244:245]
	v_med3_f32 v78, v78, s72, v197
	v_med3_f32 v79, v79, s72, v197
	v_med3_f32 v80, v80, s72, v197
	v_med3_f32 v81, v81, s72, v197
	v_med3_f32 v70, v70, s72, v197
	v_med3_f32 v71, v71, s72, v197
	v_med3_f32 v72, v72, s72, v197
	v_med3_f32 v73, v73, s72, v197
	v_med3_f32 v62, v62, s72, v197
	v_med3_f32 v63, v63, s72, v197
	v_med3_f32 v64, v64, s72, v197
	v_med3_f32 v65, v65, s72, v197
	v_med3_f32 v54, v54, s72, v197
	v_med3_f32 v55, v55, s72, v197
	v_med3_f32 v56, v56, s72, v197
	v_med3_f32 v57, v57, s72, v197
	v_cvt_pk_fp8_f32 v246, v78, v79
	v_cvt_pk_fp8_f32 v247, v70, v71
	v_cvt_pk_fp8_f32 v248, v62, v63
	v_cvt_pk_fp8_f32 v249, v54, v55
	v_add_u32_e32 v207, s75, v206
	v_add_u32_e32 v208, s76, v206
	v_cvt_pk_fp8_f32 v246, v80, v81 op_sel:[0,0,1]
	v_cvt_pk_fp8_f32 v247, v72, v73 op_sel:[0,0,1]
	v_cvt_pk_fp8_f32 v248, v64, v65 op_sel:[0,0,1]
	v_cvt_pk_fp8_f32 v249, v56, v57 op_sel:[0,0,1]
	s_nop 1
	global_store_dwordx2 v207, v[246:247], s[100:101]
	global_store_dwordx2 v208, v[248:249], s[100:101]
	v_pk_fma_f32 v[74:75], v[74:75], s[18:19], 0 op_sel_hi:[1,0,0]
	v_pk_fma_f32 v[76:77], v[76:77], s[18:19], 0 op_sel_hi:[1,0,0]
	v_pk_fma_f32 v[66:67], v[66:67], s[18:19], 0 op_sel_hi:[1,0,0]
	v_pk_fma_f32 v[68:69], v[68:69], s[18:19], 0 op_sel_hi:[1,0,0]
	v_pk_fma_f32 v[46:47], v[46:47], s[20:21], 0 op_sel_hi:[1,0,0]
	v_pk_fma_f32 v[48:49], v[48:49], s[20:21], 0 op_sel_hi:[1,0,0]
	v_pk_fma_f32 v[42:43], v[42:43], s[20:21], 0 op_sel_hi:[1,0,0]
	v_pk_fma_f32 v[44:45], v[44:45], s[20:21], 0 op_sel_hi:[1,0,0]
	v_pk_fma_f32 v[58:59], v[58:59], s[18:19], 0 op_sel_hi:[1,0,0]
	v_pk_fma_f32 v[60:61], v[60:61], s[18:19], 0 op_sel_hi:[1,0,0]
	v_pk_fma_f32 v[50:51], v[50:51], s[18:19], 0 op_sel_hi:[1,0,0]
	v_pk_fma_f32 v[52:53], v[52:53], s[18:19], 0 op_sel_hi:[1,0,0]
	v_pk_fma_f32 v[38:39], v[38:39], s[20:21], 0 op_sel_hi:[1,0,0]
	v_pk_fma_f32 v[40:41], v[40:41], s[20:21], 0 op_sel_hi:[1,0,0]
	v_pk_fma_f32 v[34:35], v[34:35], s[20:21], 0 op_sel_hi:[1,0,0]
	v_pk_fma_f32 v[36:37], v[36:37], s[20:21], 0 op_sel_hi:[1,0,0]
	v_pk_mul_f32 v[230:231], v[74:75], s[98:99] op_sel_hi:[1,0]
	v_pk_mul_f32 v[232:233], v[76:77], s[98:99] op_sel_hi:[1,0]
	v_pk_mul_f32 v[234:235], v[66:67], s[98:99] op_sel_hi:[1,0]
	v_pk_mul_f32 v[236:237], v[68:69], s[98:99] op_sel_hi:[1,0]
	v_pk_mul_f32 v[238:239], v[58:59], s[98:99] op_sel_hi:[1,0]
	v_pk_mul_f32 v[240:241], v[60:61], s[98:99] op_sel_hi:[1,0]
	v_pk_mul_f32 v[242:243], v[50:51], s[98:99] op_sel_hi:[1,0]
	v_pk_mul_f32 v[244:245], v[52:53], s[98:99] op_sel_hi:[1,0]
	v_exp_f32_e32 v230, v230
	v_exp_f32_e32 v231, v231
	v_exp_f32_e32 v232, v232
	v_exp_f32_e32 v233, v233
	v_exp_f32_e32 v234, v234
	v_exp_f32_e32 v235, v235
	v_exp_f32_e32 v236, v236
	v_exp_f32_e32 v237, v237
	v_exp_f32_e32 v238, v238
	v_exp_f32_e32 v239, v239
	v_exp_f32_e32 v240, v240
	v_exp_f32_e32 v241, v241
	v_exp_f32_e32 v242, v242
	v_exp_f32_e32 v243, v243
	v_exp_f32_e32 v244, v244
	v_exp_f32_e32 v245, v245
	v_pk_add_f32 v[230:231], v[230:231], 1.0 op_sel_hi:[1,0]
	v_pk_add_f32 v[232:233], v[232:233], 1.0 op_sel_hi:[1,0]
	v_pk_add_f32 v[234:235], v[234:235], 1.0 op_sel_hi:[1,0]
	v_pk_add_f32 v[236:237], v[236:237], 1.0 op_sel_hi:[1,0]
	v_pk_add_f32 v[238:239], v[238:239], 1.0 op_sel_hi:[1,0]
	v_pk_add_f32 v[240:241], v[240:241], 1.0 op_sel_hi:[1,0]
	v_pk_add_f32 v[242:243], v[242:243], 1.0 op_sel_hi:[1,0]
	v_pk_add_f32 v[244:245], v[244:245], 1.0 op_sel_hi:[1,0]
	v_rcp_f32_e32 v230, v230
	v_rcp_f32_e32 v231, v231
	v_rcp_f32_e32 v232, v232
	v_rcp_f32_e32 v233, v233
	v_rcp_f32_e32 v234, v234
	v_rcp_f32_e32 v235, v235
	v_rcp_f32_e32 v236, v236
	v_rcp_f32_e32 v237, v237
	v_rcp_f32_e32 v238, v238
	v_rcp_f32_e32 v239, v239
	v_rcp_f32_e32 v240, v240
	v_rcp_f32_e32 v241, v241
	v_rcp_f32_e32 v242, v242
	v_rcp_f32_e32 v243, v243
	v_rcp_f32_e32 v244, v244
	v_rcp_f32_e32 v245, v245
	v_pk_mul_f32 v[230:231], v[74:75], v[230:231]
	v_pk_mul_f32 v[232:233], v[76:77], v[232:233]
	v_pk_mul_f32 v[234:235], v[66:67], v[234:235]
	v_pk_mul_f32 v[236:237], v[68:69], v[236:237]
	v_pk_mul_f32 v[238:239], v[58:59], v[238:239]
	v_pk_mul_f32 v[240:241], v[60:61], v[240:241]
	v_pk_mul_f32 v[242:243], v[50:51], v[242:243]
	v_pk_mul_f32 v[244:245], v[52:53], v[244:245]
	v_pk_mul_f32 v[46:47], v[46:47], v[230:231]
	v_pk_mul_f32 v[48:49], v[48:49], v[232:233]
	v_pk_mul_f32 v[42:43], v[42:43], v[234:235]
	v_pk_mul_f32 v[44:45], v[44:45], v[236:237]
	v_pk_mul_f32 v[38:39], v[38:39], v[238:239]
	v_pk_mul_f32 v[40:41], v[40:41], v[240:241]
	v_pk_mul_f32 v[34:35], v[34:35], v[242:243]
	v_pk_mul_f32 v[36:37], v[36:37], v[244:245]
	v_med3_f32 v46, v46, s72, v197
	v_med3_f32 v47, v47, s72, v197
	v_med3_f32 v48, v48, s72, v197
	v_med3_f32 v49, v49, s72, v197
	v_med3_f32 v42, v42, s72, v197
	v_med3_f32 v43, v43, s72, v197
	v_med3_f32 v44, v44, s72, v197
	v_med3_f32 v45, v45, s72, v197
	v_med3_f32 v38, v38, s72, v197
	v_med3_f32 v39, v39, s72, v197
	v_med3_f32 v40, v40, s72, v197
	v_med3_f32 v41, v41, s72, v197
	v_med3_f32 v34, v34, s72, v197
	v_med3_f32 v35, v35, s72, v197
	v_med3_f32 v36, v36, s72, v197
	v_med3_f32 v37, v37, s72, v197
	v_cvt_pk_fp8_f32 v250, v46, v47
	v_cvt_pk_fp8_f32 v251, v42, v43
	v_cvt_pk_fp8_f32 v252, v38, v39
	v_cvt_pk_fp8_f32 v253, v34, v35
	v_add_u32_e32 v207, s77, v206
	v_add_u32_e32 v208, 0xf2000, v206
	v_cvt_pk_fp8_f32 v250, v48, v49 op_sel:[0,0,1]
	v_cvt_pk_fp8_f32 v251, v44, v45 op_sel:[0,0,1]
	v_cvt_pk_fp8_f32 v252, v40, v41 op_sel:[0,0,1]
	v_cvt_pk_fp8_f32 v253, v36, v37 op_sel:[0,0,1]
	s_nop 1
	global_store_dwordx2 v207, v[250:251], s[100:101]
	global_store_dwordx2 v208, v[252:253], s[100:101]
	s_andn2_b64 vcc, exec, s[2:3]
	s_mov_b64 s[2:3], -1
	s_cbranch_vccnz .LBB0_2928
	s_andn2_b64 vcc, exec, s[10:11]
	s_cbranch_vccnz .LBB0_2927
	s_barrier
	s_branch .LBB0_2927
